# conversion tickets: 2^8 weight scale folded into the f32->fp8 conversion (scaled convert, scale operand 2^-8) instead of separate multiplies
# baseline (speedup 1.0000x reference)
; __device__ __forceinline__ unsigned pk4_fp8(float a, float b, float c, float d) { int w = 0; w = __builtin_amdgcn_cvt_pk_fp8_f32(a, b, w, false); w = __builtin_amdgcn_cvt_pk_fp8_f32(c, d, w, true); return (unsigned)w; }
; #define LAS __attribute__((address_space(3)))
; #define lane (lane_id())
; __device__ __forceinline__ void cv8_to_lds(const f32x4 (&v)[16], LAS unsigned char* T, int wave, int lane) {
;     unsigned d[16];
; #pragma unroll
;     for (int i = 0; i < 16; ++i) d[i] = pg8::pk4_fp8(v[i].x * 256.f, v[i].y * 256.f, v[i].z * 256.f, v[i].w * 256.f);
;     unsigned o[4][4];
; #pragma unroll
;     for (int q = 0; q < 4; ++q) { const unsigned a = d[4 * q], b = d[4 * q + 1], c = d[4 * q + 2], e = d[4 * q + 3];
;         const unsigned t0 = __builtin_amdgcn_perm(b, a, 0x05010400u), t1 = __builtin_amdgcn_perm(b, a, 0x07030602u), t2 = __builtin_amdgcn_perm(e, c, 0x05010400u), t3 = __builtin_amdgcn_perm(e, c, 0x07030602u);
;         o[0][q] = __builtin_amdgcn_perm(t2, t0, 0x05040100u); o[1][q] = __builtin_amdgcn_perm(t2, t0, 0x07060302u); o[2][q] = __builtin_amdgcn_perm(t3, t1, 0x05040100u); o[3][q] = __builtin_amdgcn_perm(t3, t1, 0x07060302u); }
; #pragma unroll
;     for (int j = 0; j < 4; ++j) { v4u w; w.x = o[j][0]; w.y = o[j][1]; w.z = o[j][2]; w.w = o[j][3];
;         *(LAS v4u*)(T + (4 * lane + j) * 128 + 16 * (wave ^ (lane & 7))) = w; }
.LBB0_477:
	v_bitop3_b32 v130, v132, s95, 7 bitop3:0x6c
	s_xor_b64 s[40:41], s[76:77], -1
	v_lshlrev_b32_e32 v0, 9, v132
	v_lshlrev_b32_e32 v130, 4, v130
	v_add3_u32 v130, 0, v0, v130
	s_mov_b64 s[0:1], -1
	s_and_b64 vcc, exec, s[40:41]
	s_cbranch_vccz .LBB0_479
	s_mov_b32 s0, 0x3b800000
	s_waitcnt vmcnt(31)
	v_cvt_scalef32_pk_fp8_f32 v136, v66, v67, s0
	s_waitcnt vmcnt(30)
	v_cvt_scalef32_pk_fp8_f32 v137, v70, v71, s0
	v_cvt_scalef32_pk_fp8_f32 v137, v72, v73, s0 op_sel:[0,0,0,1]
	s_waitcnt vmcnt(29)
	v_cvt_scalef32_pk_fp8_f32 v138, v74, v75, s0
	s_waitcnt vmcnt(28)
	v_cvt_scalef32_pk_fp8_f32 v139, v78, v79, s0
	v_cvt_scalef32_pk_fp8_f32 v139, v80, v81, s0 op_sel:[0,0,0,1]
	s_waitcnt vmcnt(27)
	v_cvt_scalef32_pk_fp8_f32 v140, v82, v83, s0
	s_waitcnt vmcnt(26)
	v_cvt_scalef32_pk_fp8_f32 v141, v86, v87, s0
	v_cvt_scalef32_pk_fp8_f32 v141, v88, v89, s0 op_sel:[0,0,0,1]
	s_waitcnt vmcnt(25)
	v_cvt_scalef32_pk_fp8_f32 v143, v90, v91, s0
	s_waitcnt vmcnt(24)
	v_cvt_scalef32_pk_fp8_f32 v144, v94, v95, s0
	v_cvt_scalef32_pk_fp8_f32 v144, v96, v97, s0 op_sel:[0,0,0,1]
	s_waitcnt vmcnt(23)
	v_cvt_scalef32_pk_fp8_f32 v145, v98, v99, s0
	s_waitcnt vmcnt(22)
	v_cvt_scalef32_pk_fp8_f32 v148, v102, v103, s0
	v_cvt_scalef32_pk_fp8_f32 v148, v104, v105, s0 op_sel:[0,0,0,1]
	s_waitcnt vmcnt(21)
	v_cvt_scalef32_pk_fp8_f32 v149, v106, v107, s0
	s_waitcnt vmcnt(20)
	v_cvt_scalef32_pk_fp8_f32 v150, v110, v111, s0
	v_cvt_scalef32_pk_fp8_f32 v150, v112, v113, s0 op_sel:[0,0,0,1]
	s_waitcnt vmcnt(19)
	v_cvt_scalef32_pk_fp8_f32 v151, v114, v115, s0
	s_waitcnt vmcnt(18)
	v_cvt_scalef32_pk_fp8_f32 v152, v118, v119, s0
	v_cvt_scalef32_pk_fp8_f32 v136, v68, v69, s0 op_sel:[0,0,0,1]
	v_cvt_scalef32_pk_fp8_f32 v138, v76, v77, s0 op_sel:[0,0,0,1]
	v_cvt_scalef32_pk_fp8_f32 v152, v120, v121, s0 op_sel:[0,0,0,1]
	s_waitcnt vmcnt(17)
	v_cvt_scalef32_pk_fp8_f32 v140, v84, v85, s0 op_sel:[0,0,0,1]
	v_cvt_scalef32_pk_fp8_f32 v153, v122, v123, s0
	s_waitcnt vmcnt(16)
	v_cvt_scalef32_pk_fp8_f32 v143, v92, v93, s0 op_sel:[0,0,0,1]
	v_cvt_scalef32_pk_fp8_f32 v154, v126, v127, s0
	v_cvt_scalef32_pk_fp8_f32 v145, v100, v101, s0 op_sel:[0,0,0,1]
	v_cvt_scalef32_pk_fp8_f32 v149, v108, v109, s0 op_sel:[0,0,0,1]
	v_cvt_scalef32_pk_fp8_f32 v151, v116, v117, s0 op_sel:[0,0,0,1]
	v_cvt_scalef32_pk_fp8_f32 v153, v124, v125, s0 op_sel:[0,0,0,1]
	v_cvt_scalef32_pk_fp8_f32 v154, v128, v129, s0 op_sel:[0,0,0,1]
	s_mov_b32 s0, 0x5010400
	s_mov_b32 s1, 0x7030602
	v_perm_b32 v0, v137, v136, s0
	v_perm_b32 v131, v137, v136, s1
	v_perm_b32 v135, v139, v138, s0
	v_perm_b32 v136, v139, v138, s1
	s_mov_b32 s3, 0x5040100
	s_mov_b32 s2, 0x7060302
	v_perm_b32 v134, v135, v0, s3
	v_perm_b32 v138, v135, v0, s2
	v_perm_b32 v142, v136, v131, s3
	v_perm_b32 v146, v136, v131, s2
	v_perm_b32 v0, v141, v140, s0
	v_perm_b32 v131, v141, v140, s1
	v_perm_b32 v136, v144, v143, s0
	v_perm_b32 v137, v144, v143, s1
	v_perm_b32 v135, v136, v0, s3
	v_perm_b32 v139, v136, v0, s2
	v_perm_b32 v143, v137, v131, s3
	v_perm_b32 v147, v137, v131, s2
	v_perm_b32 v0, v148, v145, s0
	v_perm_b32 v131, v148, v145, s1
	v_perm_b32 v137, v150, v149, s0
	v_perm_b32 v141, v150, v149, s1
	v_perm_b32 v136, v137, v0, s3
	v_perm_b32 v140, v137, v0, s2
	v_perm_b32 v144, v141, v131, s3
	v_perm_b32 v148, v141, v131, s2
	v_perm_b32 v0, v152, v151, s0
	v_perm_b32 v141, v154, v153, s0
	v_perm_b32 v131, v152, v151, s1
	v_perm_b32 v149, v154, v153, s1
	v_perm_b32 v137, v141, v0, s3
	v_perm_b32 v141, v141, v0, s2
	v_perm_b32 v145, v149, v131, s3
	v_perm_b32 v149, v149, v131, s2
	ds_write_b128 v130, v[134:137]
	ds_write_b128 v130, v[138:141] offset:128
	ds_write_b128 v130, v[142:145] offset:256
	ds_write_b128 v130, v[146:149] offset:384
	s_waitcnt lgkmcnt(0)
	s_waitcnt lgkmcnt(0)
	s_barrier
	s_mov_b64 s[0:1], 0

; __device__ __forceinline__ unsigned pk4_fp8(float a, float b, float c, float d) { int w = 0; w = __builtin_amdgcn_cvt_pk_fp8_f32(a, b, w, false); w = __builtin_amdgcn_cvt_pk_fp8_f32(c, d, w, true); return (unsigned)w; }
; #define LAS __attribute__((address_space(3)))
; #define lane (lane_id())
; __device__ __forceinline__ void cv8_to_lds(const f32x4 (&v)[16], LAS unsigned char* T, int wave, int lane) {
;     unsigned d[16];
; #pragma unroll
;     for (int i = 0; i < 16; ++i) d[i] = pg8::pk4_fp8(v[i].x * 256.f, v[i].y * 256.f, v[i].z * 256.f, v[i].w * 256.f);
;     unsigned o[4][4];
; #pragma unroll
;     for (int q = 0; q < 4; ++q) { const unsigned a = d[4 * q], b = d[4 * q + 1], c = d[4 * q + 2], e = d[4 * q + 3];
;         const unsigned t0 = __builtin_amdgcn_perm(b, a, 0x05010400u), t1 = __builtin_amdgcn_perm(b, a, 0x07030602u), t2 = __builtin_amdgcn_perm(e, c, 0x05010400u), t3 = __builtin_amdgcn_perm(e, c, 0x07030602u);
;         o[0][q] = __builtin_amdgcn_perm(t2, t0, 0x05040100u); o[1][q] = __builtin_amdgcn_perm(t2, t0, 0x07060302u); o[2][q] = __builtin_amdgcn_perm(t3, t1, 0x05040100u); o[3][q] = __builtin_amdgcn_perm(t3, t1, 0x07060302u); }
; #pragma unroll
;     for (int j = 0; j < 4; ++j) { v4u w; w.x = o[j][0]; w.y = o[j][1]; w.z = o[j][2]; w.w = o[j][3];
;         *(LAS v4u*)(T + (4 * lane + j) * 128 + 16 * (wave ^ (lane & 7))) = w; }
.LBB0_491:
	s_xor_b64 s[28:29], s[74:75], -1
	v_readlane_b32 s48, v254, 38
	v_readlane_b32 s50, v254, 40
	v_readlane_b32 s52, v254, 42
	v_readlane_b32 s53, v254, 43
	s_mov_b64 s[0:1], -1
	s_and_b64 vcc, exec, s[28:29]
	v_readlane_b32 s49, v254, 39
	v_readlane_b32 s51, v254, 41
	s_cbranch_vccz .LBB0_495
	s_mov_b32 s0, 0x3b800000
	s_waitcnt vmcnt(15)
	v_cvt_scalef32_pk_fp8_f32 v108, v2, v3, s0
	s_waitcnt vmcnt(14)
	v_cvt_scalef32_pk_fp8_f32 v109, v6, v7, s0
	v_cvt_scalef32_pk_fp8_f32 v109, v8, v9, s0 op_sel:[0,0,0,1]
	s_waitcnt vmcnt(13)
	v_cvt_scalef32_pk_fp8_f32 v110, v10, v11, s0
	s_waitcnt vmcnt(12)
	v_cvt_scalef32_pk_fp8_f32 v111, v14, v15, s0
	v_cvt_scalef32_pk_fp8_f32 v111, v16, v17, s0 op_sel:[0,0,0,1]
	s_waitcnt vmcnt(11)
	v_cvt_scalef32_pk_fp8_f32 v112, v18, v19, s0
	s_waitcnt vmcnt(10)
	v_cvt_scalef32_pk_fp8_f32 v113, v22, v23, s0
	v_cvt_scalef32_pk_fp8_f32 v113, v24, v25, s0 op_sel:[0,0,0,1]
	s_waitcnt vmcnt(9)
	v_cvt_scalef32_pk_fp8_f32 v115, v26, v27, s0
	s_waitcnt vmcnt(8)
	v_cvt_scalef32_pk_fp8_f32 v116, v30, v31, s0
	v_cvt_scalef32_pk_fp8_f32 v116, v32, v33, s0 op_sel:[0,0,0,1]
	s_waitcnt vmcnt(7)
	v_cvt_scalef32_pk_fp8_f32 v117, v34, v35, s0
	s_waitcnt vmcnt(6)
	v_cvt_scalef32_pk_fp8_f32 v120, v38, v39, s0
	v_cvt_scalef32_pk_fp8_f32 v120, v40, v41, s0 op_sel:[0,0,0,1]
	s_waitcnt vmcnt(5)
	v_cvt_scalef32_pk_fp8_f32 v121, v42, v43, s0
	s_waitcnt vmcnt(4)
	v_cvt_scalef32_pk_fp8_f32 v122, v46, v47, s0
	v_cvt_scalef32_pk_fp8_f32 v122, v48, v49, s0 op_sel:[0,0,0,1]
	s_waitcnt vmcnt(3)
	v_cvt_scalef32_pk_fp8_f32 v123, v50, v51, s0
	s_waitcnt vmcnt(2)
	v_cvt_scalef32_pk_fp8_f32 v124, v54, v55, s0
	v_cvt_scalef32_pk_fp8_f32 v108, v4, v5, s0 op_sel:[0,0,0,1]
	v_cvt_scalef32_pk_fp8_f32 v110, v12, v13, s0 op_sel:[0,0,0,1]
	v_cvt_scalef32_pk_fp8_f32 v124, v56, v57, s0 op_sel:[0,0,0,1]
	s_waitcnt vmcnt(1)
	v_cvt_scalef32_pk_fp8_f32 v112, v20, v21, s0 op_sel:[0,0,0,1]
	v_cvt_scalef32_pk_fp8_f32 v125, v58, v59, s0
	s_waitcnt vmcnt(0)
	v_cvt_scalef32_pk_fp8_f32 v115, v28, v29, s0 op_sel:[0,0,0,1]
	v_cvt_scalef32_pk_fp8_f32 v126, v62, v63, s0
	v_cvt_scalef32_pk_fp8_f32 v117, v36, v37, s0 op_sel:[0,0,0,1]
	v_cvt_scalef32_pk_fp8_f32 v121, v44, v45, s0 op_sel:[0,0,0,1]
	v_cvt_scalef32_pk_fp8_f32 v123, v52, v53, s0 op_sel:[0,0,0,1]
	v_cvt_scalef32_pk_fp8_f32 v125, v60, v61, s0 op_sel:[0,0,0,1]
	v_cvt_scalef32_pk_fp8_f32 v126, v64, v65, s0 op_sel:[0,0,0,1]
	s_mov_b32 s0, 0x5010400
	s_mov_b32 s1, 0x7030602
	v_perm_b32 v67, v109, v108, s0
	v_perm_b32 v105, v109, v108, s1
	v_perm_b32 v107, v111, v110, s0
	v_perm_b32 v108, v111, v110, s1
	s_mov_b32 s4, 0x5040100
	s_mov_b32 s3, 0x7060302
	v_perm_b32 v106, v107, v67, s4
	v_perm_b32 v110, v107, v67, s3
	v_perm_b32 v114, v108, v105, s4
	v_perm_b32 v118, v108, v105, s3
	v_perm_b32 v67, v113, v112, s0
	v_perm_b32 v105, v113, v112, s1
	v_perm_b32 v108, v116, v115, s0
	v_perm_b32 v109, v116, v115, s1
	v_perm_b32 v107, v108, v67, s4
	v_perm_b32 v111, v108, v67, s3
	v_perm_b32 v115, v109, v105, s4
	v_perm_b32 v119, v109, v105, s3
	v_perm_b32 v67, v120, v117, s0
	v_perm_b32 v105, v120, v117, s1
	v_perm_b32 v109, v122, v121, s0
	v_perm_b32 v113, v122, v121, s1
	v_perm_b32 v108, v109, v67, s4
	v_perm_b32 v112, v109, v67, s3
	v_perm_b32 v116, v113, v105, s4
	v_perm_b32 v120, v113, v105, s3
	v_perm_b32 v67, v124, v123, s0
	v_perm_b32 v113, v126, v125, s0
	v_perm_b32 v105, v124, v123, s1
	v_perm_b32 v121, v126, v125, s1
	v_perm_b32 v109, v113, v67, s4
	v_perm_b32 v113, v113, v67, s3
	v_add_u32_e32 v67, s22, v130
	v_perm_b32 v117, v121, v105, s4
	v_perm_b32 v121, v121, v105, s3
	ds_write_b128 v67, v[106:109]
	ds_write_b128 v67, v[110:113] offset:128
	ds_write_b128 v67, v[114:117] offset:256
	ds_write_b128 v67, v[118:121] offset:384
	s_waitcnt lgkmcnt(0)
	s_waitcnt lgkmcnt(0)
	s_barrier
	s_cbranch_execz .LBB0_496
